# n22_ld4
# speedup vs baseline: 1.0040x; 1.0040x over previous
.Lrec_own_ok:
	s_barrier
	ds_read_b128 v[194:197], v180
	ds_read_b128 v[198:201], v181
	ds_read_b128 v[202:205], v182
	ds_read_b128 v[206:209], v183
	s_cmp_eq_u32 s59, 0
	s_cbranch_scc1 .Lrec_tail1
.Lrec_tail0:
	s_waitcnt lgkmcnt(3)
	v_mfma_f32_16x16x32_f16 v[154:157], v[82:85], v[194:197], v[154:157]
	ds_read_b128 v[210:213], v184
	s_waitcnt lgkmcnt(3)
	v_mfma_f32_16x16x32_f16 v[154:157], v[86:89], v[198:201], v[154:157]
	ds_read_b128 v[214:217], v185
	global_load_dwordx2 v[174:175], v243, s[52:53] nt
	s_waitcnt lgkmcnt(3)
	v_mfma_f32_16x16x32_f16 v[154:157], v[90:93], v[202:205], v[154:157]
	ds_read_b128 v[218:221], v186
	global_store_dword v242, v193, s[48:49] nt
	s_waitcnt lgkmcnt(3)
	v_mfma_f32_16x16x32_f16 v[154:157], v[94:97], v[206:209], v[154:157]
	ds_read_b128 v[222:225], v187
	s_mov_b64 exec, s[2:3]
	s_cmp_lg_u32 s57, 0
	s_cbranch_scc1 .Lrec_poi_sc1_0
	buffer_store_dwordx2 v[172:173], v165, s[8:11], s46 offen
	s_branch .Lrec_poi_done_0

.Lrec_poi_done_0:
	s_mov_b64 exec, -1
	s_waitcnt lgkmcnt(3)
	v_mfma_f32_16x16x32_f16 v[154:157], v[98:101], v[210:213], v[154:157]
	ds_read_b128 v[226:229], v188
	s_waitcnt lgkmcnt(3)
	v_mfma_f32_16x16x32_f16 v[154:157], v[102:105], v[214:217], v[154:157]
	ds_read_b128 v[230:233], v189
	s_xor_b32 s42, s42, 0x8000
	s_mov_b32 m0, s42
	s_and_b32 s36, s33, 7
	s_lshl_b32 s36, s36, 18
	s_add_u32 s40, s54, s36
	s_addc_u32 s41, s55, 0
	s_waitcnt lgkmcnt(3)
	v_mfma_f32_16x16x32_f16 v[154:157], v[106:109], v[218:221], v[154:157]
	ds_read_b128 v[234:237], v190
	s_add_i32 s58, s33, 1
	s_and_b32 s58, s58, 7
	s_lshl_b32 s58, s58, 18
	s_add_i32 s46, s33, 6
	s_and_b32 s46, s46, 7
	s_lshl_b32 s46, s46, 18
	s_waitcnt lgkmcnt(3)
	v_mfma_f32_16x16x32_f16 v[154:157], v[110:113], v[222:225], v[154:157]
	ds_read_b128 v[238:241], v191
	s_add_u32 s48, s48, 0x80000
	s_addc_u32 s49, s49, 0
	s_add_i32 s36, s33, 2
	s_min_u32 s36, s36, 0xff
	s_lshr_b32 s37, s36, 1
	s_lshl_b32 s37, s37, 21
	s_waitcnt lgkmcnt(3)
	v_mfma_f32_16x16x32_f16 v[154:157], v[114:117], v[226:229], v[154:157]
	s_and_b32 s36, s36, 1
	s_lshl_b32 s36, s36, 3
	s_or_b32 s37, s37, s36
	s_add_u32 s52, s50, s37
	s_addc_u32 s53, s51, 0
	s_waitcnt lgkmcnt(2)
	v_mfma_f32_16x16x32_f16 v[154:157], v[118:121], v[230:233], v[154:157]
	s_waitcnt lgkmcnt(1)
	v_mfma_f32_16x16x32_f16 v[154:157], v[122:125], v[234:237], v[154:157]
	s_waitcnt lgkmcnt(0)
	v_mfma_f32_16x16x32_f16 v[154:157], v[126:129], v[238:241], v[154:157]
	v_mfma_f32_16x16x32_f16 v[158:161], v[18:21], v[194:197], v[158:161]
	v_mfma_f32_16x16x32_f16 v[158:161], v[22:25], v[198:201], v[158:161]
	v_mfma_f32_16x16x32_f16 v[158:161], v[26:29], v[202:205], v[158:161]
	v_mfma_f32_16x16x32_f16 v[158:161], v[30:33], v[206:209], v[158:161]
	s_nop 3
	ds_write_b128 v178, v[154:157]
	v_mfma_f32_16x16x32_f16 v[158:161], v[34:37], v[210:213], v[158:161]
	v_mfma_f32_16x16x32_f16 v[158:161], v[38:41], v[214:217], v[158:161]
	v_mfma_f32_16x16x32_f16 v[158:161], v[42:45], v[218:221], v[158:161]
	v_mfma_f32_16x16x32_f16 v[158:161], v[46:49], v[222:225], v[158:161]
	s_waitcnt lgkmcnt(0)
	s_barrier
	ds_read_b128 v[194:197], v179
	v_mfma_f32_16x16x32_f16 v[158:161], v[50:53], v[226:229], v[158:161]
	v_mfma_f32_16x16x32_f16 v[158:161], v[54:57], v[230:233], v[158:161]
	v_mfma_f32_16x16x32_f16 v[158:161], v[58:61], v[234:237], v[158:161]
	v_mfma_f32_16x16x32_f16 v[158:161], v[62:65], v[238:241], v[158:161]
	s_nop 7
	v_pk_add_f32 v[198:199], v[158:159], v[250:251]
	v_pk_add_f32 v[200:201], v[160:161], v[252:253]
	s_branch .Lrec_act
.Lrec_tail1:
	s_waitcnt lgkmcnt(3)
	v_mfma_f32_16x16x32_f16 v[158:161], v[18:21], v[194:197], v[158:161]
	ds_read_b128 v[210:213], v184
	s_waitcnt lgkmcnt(3)
	v_mfma_f32_16x16x32_f16 v[158:161], v[22:25], v[198:201], v[158:161]
	ds_read_b128 v[214:217], v185
	global_load_dwordx2 v[174:175], v243, s[52:53] nt
	s_waitcnt lgkmcnt(3)
	v_mfma_f32_16x16x32_f16 v[158:161], v[26:29], v[202:205], v[158:161]
	ds_read_b128 v[218:221], v186
	global_store_dword v242, v193, s[48:49] nt
	s_waitcnt lgkmcnt(3)
	v_mfma_f32_16x16x32_f16 v[158:161], v[30:33], v[206:209], v[158:161]
	ds_read_b128 v[222:225], v187
	s_mov_b64 exec, s[2:3]
	s_cmp_lg_u32 s57, 0
	s_cbranch_scc1 .Lrec_poi_sc1_1
	buffer_store_dwordx2 v[172:173], v165, s[8:11], s46 offen
	s_branch .Lrec_poi_done_1

.Lrec_poi_done_1:
	s_mov_b64 exec, -1
	s_waitcnt lgkmcnt(3)
	v_mfma_f32_16x16x32_f16 v[158:161], v[34:37], v[210:213], v[158:161]
	ds_read_b128 v[226:229], v188
	s_waitcnt lgkmcnt(3)
	v_mfma_f32_16x16x32_f16 v[158:161], v[38:41], v[214:217], v[158:161]
	ds_read_b128 v[230:233], v189
	s_xor_b32 s42, s42, 0x8000
	s_mov_b32 m0, s42
	s_and_b32 s36, s33, 7
	s_lshl_b32 s36, s36, 18
	s_add_u32 s40, s54, s36
	s_addc_u32 s41, s55, 0
	s_waitcnt lgkmcnt(3)
	v_mfma_f32_16x16x32_f16 v[158:161], v[42:45], v[218:221], v[158:161]
	ds_read_b128 v[234:237], v190
	s_add_i32 s58, s33, 1
	s_and_b32 s58, s58, 7
	s_lshl_b32 s58, s58, 18
	s_add_i32 s46, s33, 6
	s_and_b32 s46, s46, 7
	s_lshl_b32 s46, s46, 18
	s_waitcnt lgkmcnt(3)
	v_mfma_f32_16x16x32_f16 v[158:161], v[46:49], v[222:225], v[158:161]
	ds_read_b128 v[238:241], v191
	s_add_u32 s48, s48, 0x80000
	s_addc_u32 s49, s49, 0
	s_add_i32 s36, s33, 2
	s_min_u32 s36, s36, 0xff
	s_lshr_b32 s37, s36, 1
	s_lshl_b32 s37, s37, 21
	s_waitcnt lgkmcnt(3)
	v_mfma_f32_16x16x32_f16 v[158:161], v[50:53], v[226:229], v[158:161]
	s_and_b32 s36, s36, 1
	s_lshl_b32 s36, s36, 3
	s_or_b32 s37, s37, s36
	s_add_u32 s52, s50, s37
	s_addc_u32 s53, s51, 0
	s_waitcnt lgkmcnt(2)
	v_mfma_f32_16x16x32_f16 v[158:161], v[54:57], v[230:233], v[158:161]
	s_waitcnt lgkmcnt(1)
	v_mfma_f32_16x16x32_f16 v[158:161], v[58:61], v[234:237], v[158:161]
	s_waitcnt lgkmcnt(0)
	v_mfma_f32_16x16x32_f16 v[158:161], v[62:65], v[238:241], v[158:161]
	v_mfma_f32_16x16x32_f16 v[154:157], v[82:85], v[194:197], v[154:157]
	v_mfma_f32_16x16x32_f16 v[154:157], v[86:89], v[198:201], v[154:157]
	v_mfma_f32_16x16x32_f16 v[154:157], v[90:93], v[202:205], v[154:157]
	v_mfma_f32_16x16x32_f16 v[154:157], v[94:97], v[206:209], v[154:157]
	s_nop 3
	ds_write_b128 v178, v[158:161]
	v_mfma_f32_16x16x32_f16 v[154:157], v[98:101], v[210:213], v[154:157]
	v_mfma_f32_16x16x32_f16 v[154:157], v[102:105], v[214:217], v[154:157]
	v_mfma_f32_16x16x32_f16 v[154:157], v[106:109], v[218:221], v[154:157]
	v_mfma_f32_16x16x32_f16 v[154:157], v[110:113], v[222:225], v[154:157]
	s_waitcnt lgkmcnt(0)
	s_barrier
	ds_read_b128 v[194:197], v179
	v_mfma_f32_16x16x32_f16 v[154:157], v[114:117], v[226:229], v[154:157]
	v_mfma_f32_16x16x32_f16 v[154:157], v[118:121], v[230:233], v[154:157]
	v_mfma_f32_16x16x32_f16 v[154:157], v[122:125], v[234:237], v[154:157]
	v_mfma_f32_16x16x32_f16 v[154:157], v[126:129], v[238:241], v[154:157]
	s_nop 7
	v_pk_add_f32 v[198:199], v[154:155], v[250:251]
	v_pk_add_f32 v[200:201], v[156:157], v[252:253]
